# expert-down epilogue: LDS staging rows XOR-swizzled (8-way -> 2-way bank conflict on the 8-byte staging writes)
# speedup vs baseline: 1.0149x; 1.0149x over previous
; #define LAS __attribute__((address_space(3)))
; #define PG8_STAGE(bufoff, gbase, voff) do { _Pragma("unroll") for (int _i = 0; _i < 2; ++_i) \
;         __builtin_amdgcn_global_load_lds((const GAS unsigned*)((const GAS char*)(gbase) + (voff)[_i]), (LAS unsigned*)(lds + (bufoff) + ldsw + _i * 8192), 16, 0, 0); } while (0)
; #define PG8_WAIT_V(n) asm volatile("s_waitcnt vmcnt(" #n ")" ::: "memory")
; #define PG8_BAR __builtin_amdgcn_s_barrier()
; template <class Epi, class Sched, bool GATHER, bool FP8 = false, bool UNI = false>
; __device__ __forceinline__ void gemm_phase(LAS unsigned char* lds, const Sched& S, const Epi& E) {
;     ...
;         PG8_STAGE(PG8_SB(0, 0), cB, boc); PG8_STAGE(PG8_SB(0, 1), cB + hB, boc); PG8_STAGE(PG8_SA(0, 0), cA, aoc[0]); PG8_STAGE(PG8_SA(0, 1), cA, aoc[1]);
;         if (wr == 1) PG8_BAR;
;         PG8_WAIT_V(2); PG8_BAR;
;         PG8_STAGE(PG8_SB(1, 0), cB + 128, boc); PG8_STAGE(PG8_SA(1, 0), cA + 128, aoc[0]); PG8_STAGE(PG8_SB(1, 1), cB + hB + 128, boc);
;         PG8_WAIT_V(6); PG8_BAR;
;     __device__ __forceinline__ bool operator()(f32x4 (&acc)[2][2][4][2], const Unit& u, int wr, int wc, int fr, int fq, LAS unsigned char* scr) const {
;         const int lane = fq * 16 + fr, rowb = u.row0 + wr * 64, colb = u.col0 + wc * 64;
; #pragma unroll
;         for (int ai = 0; ai < 2; ++ai)
; #pragma unroll
;             for (int m = 0; m < 4; ++m) { const size_t rg = (size_t)(rowb + ai * 128 + m * 16);
;                 if constexpr (F8OUT) {
;                     LAS unsigned char* sb = scr + ((ai * 4 + m) & 1) * 1024;
; #pragma unroll
;                     for (int bj = 0; bj < 2; ++bj) { const f32x4 v0 = acc[ai][bj][m][0], v1 = acc[ai][bj][m][1]; u32x2 w8;
;                         int q = __builtin_amdgcn_cvt_pk_fp8_f32(v0[0], v0[1], 0, false); q = __builtin_amdgcn_cvt_pk_fp8_f32(v0[2], v0[3], q, true); w8.x = (unsigned)q;
;                         q = __builtin_amdgcn_cvt_pk_fp8_f32(v1[0], v1[1], 0, false); q = __builtin_amdgcn_cvt_pk_fp8_f32(v1[2], v1[3], q, true); w8.y = (unsigned)q;
;                         *(LAS u32x2*)(sb + fr * 64 + bj * 32 + fq * 8) = w8; }
;                     const int r = lane >> 2, ch = lane & 3; const u32x4 o = *(const LAS u32x4*)(sb + r * 64 + ch * 16);
.LBB0_1944:
	s_lshl_b32 s68, s12, 8
	s_lshl_b32 s69, s10, 8
	s_and_b32 s29, s15, 3
	s_lshl_b32 s49, s19, 6
	s_add_u32 s8, s8, 0x3fb00000
	s_addc_u32 s9, s9, 0
	s_add_i32 s30, s16, 0x18000
	s_add_i32 s50, s30, s26
	s_mov_b64 s[10:11], 0x80
	v_lshl_add_u64 v[8:9], v[8:9], 0, s[10:11]
	s_mov_b32 m0, s50
	s_add_i32 s51, s50, 0x2000
	s_add_i32 s56, s45, 0x8000
	s_add_i32 s57, s45, 0xa000
	s_waitcnt vmcnt(2)
	s_barrier
	global_load_lds_dwordx4 v[8:9], off
	v_lshl_add_u64 v[6:7], v[6:7], 0, s[10:11]
	s_mov_b32 m0, s51
	s_add_u32 s12, s22, 0x4080
	global_load_lds_dwordx4 v[6:7], off
	v_lshl_add_u64 v[2:3], v[2:3], 0, s[10:11]
	s_mov_b32 m0, s56
	s_addc_u32 s13, s23, 0
	s_add_i32 s31, s16, 0x1c000
	global_load_lds_dwordx4 v[2:3], off
	v_lshl_add_u64 v[2:3], v[4:5], 0, s[10:11]
	s_mov_b32 m0, s57
	s_add_i32 s58, s31, s26
	global_load_lds_dwordx4 v[2:3], off
	v_lshl_add_u64 v[2:3], s[12:13], 0, v[162:163]
	s_mov_b32 m0, s58
	s_add_i32 s59, s58, 0x2000
	global_load_lds_dwordx4 v[2:3], off
	v_lshl_add_u64 v[2:3], s[12:13], 0, v[168:169]
	s_mov_b32 m0, s59
	v_lshlrev_b32_e32 v5, 1, v1
	global_load_lds_dwordx4 v[2:3], off
	v_lshlrev_b32_e32 v3, 6, v1
	s_cmpk_lt_u32 s14, 0x100
	v_and_b32_e32 v3, 0x3c0, v3
	v_lshlrev_b32_e32 v4, 2, v1
	v_and_b32_e32 v5, 32, v5
	v_lshlrev_b32_e32 v7, 5, v1
	s_cselect_b64 s[12:13], -1, 0
	s_lshl_b32 s14, s15, 11
	v_and_b32_e32 v4, 32, v4
	v_or_b32_e32 v6, v3, v5
	v_and_b32_e32 v7, 0x400, v7
	s_add_i32 s14, s16, s14
	v_lshrrev_b32_e32 v2, 1, v1
	v_lshl_or_b32 v8, s19, 13, v7
	v_bitop3_b32 v5, v3, v4, v5 bitop3:0x36
	v_bitop3_b32 v4, v6, v4, 16 bitop3:0x36
	v_lshl_or_b32 v7, s29, 12, v7
	s_waitcnt vmcnt(6)
	s_add_i32 s14, s14, 0x20000
	s_lshl_b32 s60, s29, 6
	v_bfe_u32 v174, v1, 2, 4
	s_add_i32 s61, s16, 0x24104
	s_ashr_i32 s62, s18, 3
	s_and_b32 s63, s17, 7
	s_ashr_i32 s64, s17, 3
	v_and_b32_e32 v2, 24, v2
	v_or_b32_e32 v9, v5, v8
	v_or_b32_e32 v6, v4, v8
	v_or_b32_e32 v5, v5, v7
	v_or_b32_e32 v4, v4, v7
	v_and_b32_e32 v176, 48, v10
	v_add_u32_e32 v3, s14, v3
	v_lshl_add_u32 v7, v174, 6, s14
	s_cmp_lt_i32 s64, s62
	v_mov_b32_e32 v167, v163
	v_mov_b32_e32 v173, v163
	v_mov_b32_e32 v175, v163
	v_mov_b32_e32 v177, v163
	s_mov_b32 s65, 0
	s_cselect_b64 s[14:15], -1, 0
	v_add_u32_e32 v1, s27, v5
	v_add_u32_e32 v186, s27, v4
	v_add_u32_e32 v187, s28, v5
	v_add_u32_e32 v188, s28, v4
	v_add_u32_e32 v189, s16, v9
	v_add_u32_e32 v190, s16, v6
	v_mov_b32_e32 v191, 0x79
	v_mov_b32_e32 v192, 0x7f
	v_add_u32_e32 v193, s30, v5
	v_add_u32_e32 v194, s30, v4
	v_add_u32_e32 v195, s31, v5
	v_add_u32_e32 v196, s31, v4
	v_mbcnt_lo_u32_b32 v255, -1, 0
	v_mbcnt_hi_u32_b32 v255, -1, v255
	v_and_b32_e32 v255, 16, v255
	v_xor_b32_e32 v1, v1, v255
	v_xor_b32_e32 v186, v186, v255
	v_xor_b32_e32 v187, v187, v255
	v_xor_b32_e32 v188, v188, v255
	v_xor_b32_e32 v189, v189, v255
	v_xor_b32_e32 v190, v190, v255
	v_xor_b32_e32 v193, v193, v255
	v_xor_b32_e32 v194, v194, v255
	v_xor_b32_e32 v195, v195, v255
	v_xor_b32_e32 v196, v196, v255
	v_add_u32_e32 v197, v3, v2
	v_add_u32_e32 v198, v7, v176
	v_lshrrev_b32_e32 v255, 3, v197
	v_and_b32_e32 v255, 0x30, v255
	v_xor_b32_e32 v197, v197, v255
	v_lshrrev_b32_e32 v255, 3, v198
	v_and_b32_e32 v255, 0x30, v255
	v_xor_b32_e32 v198, v198, v255
	v_xor_b32_e32 v255, 32, v197
	s_barrier
	s_waitcnt vmcnt(0)
	s_branch .LBB0_1947

; #define GAS __attribute__((address_space(1)))
; #define LAS __attribute__((address_space(3)))
;     __device__ __forceinline__ bool operator()(f32x4 (&acc)[2][2][4][2], const Unit& u, int wr, int wc, int fr, int fq, LAS unsigned char* scr) const {
;     ...
;         for (int ai = 0; ai < 2; ++ai)
; #pragma unroll
;             for (int m = 0; m < 4; ++m) { const size_t rg = (size_t)(rowb + ai * 128 + m * 16);
;                 if constexpr (F8OUT) {
;                     LAS unsigned char* sb = scr + ((ai * 4 + m) & 1) * 1024;
; #pragma unroll
;                     for (int bj = 0; bj < 2; ++bj) { const f32x4 v0 = acc[ai][bj][m][0], v1 = acc[ai][bj][m][1]; u32x2 w8;
;                         int q = __builtin_amdgcn_cvt_pk_fp8_f32(v0[0], v0[1], 0, false); q = __builtin_amdgcn_cvt_pk_fp8_f32(v0[2], v0[3], q, true); w8.x = (unsigned)q;
;                         q = __builtin_amdgcn_cvt_pk_fp8_f32(v1[0], v1[1], 0, false); q = __builtin_amdgcn_cvt_pk_fp8_f32(v1[2], v1[3], q, true); w8.y = (unsigned)q;
;                         *(LAS u32x2*)(sb + fr * 64 + bj * 32 + fq * 8) = w8; }
;                     const int r = lane >> 2, ch = lane & 3; const u32x4 o = *(const LAS u32x4*)(sb + r * 64 + ch * 16);
;                     *(GAS u32x4*)((GAS unsigned char*)Y + (rg + r) * D_MODEL + colb + ch * 16) = o;
.LBB0_1964:
	v_mov_b32_e32 v2, 0
	v_mov_b32_e32 v3, 0
	v_cvt_pk_fp8_f32 v2, v158, v159
	v_cvt_pk_fp8_f32 v3, v154, v155
	v_mov_b32_e32 v4, 0
	v_mov_b32_e32 v5, 0
	v_cvt_pk_fp8_f32 v4, v150, v151
	v_cvt_pk_fp8_f32 v5, v146, v147
	v_cvt_pk_fp8_f32 v2, v160, v161 op_sel:[0,0,1]
	v_cvt_pk_fp8_f32 v3, v156, v157 op_sel:[0,0,1]
	v_cvt_pk_fp8_f32 v4, v152, v153 op_sel:[0,0,1]
	v_cvt_pk_fp8_f32 v5, v148, v149 op_sel:[0,0,1]
	v_mov_b32_e32 v8, 0
	v_mov_b32_e32 v9, 0
	v_cvt_pk_fp8_f32 v8, v142, v143
	v_cvt_pk_fp8_f32 v9, v138, v139
	v_mov_b32_e32 v10, 0
	v_mov_b32_e32 v11, 0
	s_add_i32 s20, s69, s49
	v_cvt_pk_fp8_f32 v10, v134, v135
	v_cvt_pk_fp8_f32 v11, v130, v131
	ds_write_b64 v197, v[2:3]
	ds_write_b64 v255, v[4:5]
	s_ashr_i32 s21, s20, 31
	ds_read_b128 v[2:5], v198
	v_lshl_add_u64 v[6:7], s[20:21], 0, v[174:175]
	s_add_i32 s22, s68, s60
	v_lshlrev_b64 v[6:7], 11, v[6:7]
	v_cvt_pk_fp8_f32 v8, v144, v145 op_sel:[0,0,1]
	v_cvt_pk_fp8_f32 v9, v140, v141 op_sel:[0,0,1]
	s_ashr_i32 s23, s22, 31
	v_lshl_add_u64 v[6:7], s[8:9], 0, v[6:7]
	v_cvt_pk_fp8_f32 v10, v136, v137 op_sel:[0,0,1]
	v_cvt_pk_fp8_f32 v11, v132, v133 op_sel:[0,0,1]
	v_lshl_add_u64 v[6:7], v[6:7], 0, s[22:23]
	v_lshl_add_u64 v[12:13], v[6:7], 0, v[176:177]
	ds_write_b64 v197, v[8:9] offset:1024
	ds_write_b64 v255, v[10:11] offset:1024
	s_waitcnt lgkmcnt(0)
	global_store_dwordx4 v[12:13], v[2:5], off
	s_add_i32 s28, s20, 16
	v_mov_b32_e32 v10, 0
	v_mov_b32_e32 v4, 0
	v_mov_b32_e32 v5, 0
	v_cvt_pk_fp8_f32 v4, v126, v127
	v_cvt_pk_fp8_f32 v5, v122, v123
	v_mov_b32_e32 v11, 0
	s_ashr_i32 s29, s28, 31
	v_cvt_pk_fp8_f32 v10, v118, v119
	v_cvt_pk_fp8_f32 v11, v114, v115
	ds_read_b128 v[6:9], v198 offset:1024
	v_lshl_add_u64 v[2:3], s[28:29], 0, v[174:175]
	v_lshlrev_b64 v[2:3], 11, v[2:3]
	v_lshl_add_u64 v[2:3], s[8:9], 0, v[2:3]
	v_cvt_pk_fp8_f32 v4, v128, v129 op_sel:[0,0,1]
	v_cvt_pk_fp8_f32 v5, v124, v125 op_sel:[0,0,1]
	v_lshl_add_u64 v[2:3], v[2:3], 0, s[22:23]
	v_cvt_pk_fp8_f32 v10, v120, v121 op_sel:[0,0,1]
	v_cvt_pk_fp8_f32 v11, v116, v117 op_sel:[0,0,1]
	v_lshl_add_u64 v[2:3], v[2:3], 0, v[176:177]
	s_waitcnt lgkmcnt(0)
	global_store_dwordx4 v[2:3], v[6:9], off
	ds_write_b64 v197, v[4:5]
	ds_write_b64 v255, v[10:11]
	v_mov_b32_e32 v8, 0
	v_mov_b32_e32 v9, 0
	v_cvt_pk_fp8_f32 v8, v106, v107
	v_cvt_pk_fp8_f32 v9, v98, v99
	v_mov_b32_e32 v10, 0
	v_mov_b32_e32 v11, 0
	s_add_i32 s28, s20, 32
	v_cvt_pk_fp8_f32 v10, v86, v87
	v_cvt_pk_fp8_f32 v11, v82, v83
	s_ashr_i32 s29, s28, 31
	ds_read_b128 v[2:5], v198
	v_lshl_add_u64 v[6:7], s[28:29], 0, v[174:175]
	v_lshlrev_b64 v[6:7], 11, v[6:7]
	v_cvt_pk_fp8_f32 v8, v108, v109 op_sel:[0,0,1]
	v_cvt_pk_fp8_f32 v9, v100, v101 op_sel:[0,0,1]
	v_lshl_add_u64 v[6:7], s[8:9], 0, v[6:7]
	v_cvt_pk_fp8_f32 v10, v88, v89 op_sel:[0,0,1]
	v_cvt_pk_fp8_f32 v11, v84, v85 op_sel:[0,0,1]
	v_lshl_add_u64 v[6:7], v[6:7], 0, s[22:23]
	v_lshl_add_u64 v[12:13], v[6:7], 0, v[176:177]
	ds_write_b64 v197, v[8:9] offset:1024
	ds_write_b64 v255, v[10:11] offset:1024
	s_waitcnt lgkmcnt(0)
	global_store_dwordx4 v[12:13], v[2:5], off
	s_add_i32 s28, s20, 48
	v_mov_b32_e32 v10, 0
	v_mov_b32_e32 v4, 0
	v_mov_b32_e32 v5, 0
	v_cvt_pk_fp8_f32 v4, v70, v71
	v_cvt_pk_fp8_f32 v5, v66, v67
	v_mov_b32_e32 v11, 0
	s_ashr_i32 s29, s28, 31
	v_cvt_pk_fp8_f32 v10, v102, v103
	v_cvt_pk_fp8_f32 v11, v110, v111
	ds_read_b128 v[6:9], v198 offset:1024
	v_lshl_add_u64 v[2:3], s[28:29], 0, v[174:175]
	v_lshlrev_b64 v[2:3], 11, v[2:3]
	v_lshl_add_u64 v[2:3], s[8:9], 0, v[2:3]
	v_cvt_pk_fp8_f32 v4, v72, v73 op_sel:[0,0,1]
	v_cvt_pk_fp8_f32 v5, v68, v69 op_sel:[0,0,1]
	v_lshl_add_u64 v[2:3], v[2:3], 0, s[22:23]
	v_cvt_pk_fp8_f32 v10, v104, v105 op_sel:[0,0,1]
	v_cvt_pk_fp8_f32 v11, v112, v113 op_sel:[0,0,1]
	v_lshl_add_u64 v[2:3], v[2:3], 0, v[176:177]
	s_waitcnt lgkmcnt(0)
	global_store_dwordx4 v[2:3], v[6:9], off
	ds_write_b64 v197, v[4:5]
	ds_write_b64 v255, v[10:11]
	v_mov_b32_e32 v8, 0
	v_mov_b32_e32 v9, 0
	v_cvt_pk_fp8_f32 v8, v38, v39
	v_cvt_pk_fp8_f32 v9, v34, v35
	v_mov_b32_e32 v10, 0
	v_mov_b32_e32 v11, 0
	s_add_i32 s28, s20, 0x80
	v_cvt_pk_fp8_f32 v10, v90, v91
	v_cvt_pk_fp8_f32 v11, v94, v95
	s_ashr_i32 s29, s28, 31
	ds_read_b128 v[2:5], v198
	v_lshl_add_u64 v[6:7], s[28:29], 0, v[174:175]
	v_lshlrev_b64 v[6:7], 11, v[6:7]
	v_cvt_pk_fp8_f32 v8, v40, v41 op_sel:[0,0,1]
	v_cvt_pk_fp8_f32 v9, v36, v37 op_sel:[0,0,1]
	v_lshl_add_u64 v[6:7], s[8:9], 0, v[6:7]
	v_cvt_pk_fp8_f32 v10, v92, v93 op_sel:[0,0,1]
	v_cvt_pk_fp8_f32 v11, v96, v97 op_sel:[0,0,1]
	v_lshl_add_u64 v[6:7], v[6:7], 0, s[22:23]
	v_lshl_add_u64 v[12:13], v[6:7], 0, v[176:177]
	ds_write_b64 v197, v[8:9] offset:1024
	ds_write_b64 v255, v[10:11] offset:1024
	s_waitcnt lgkmcnt(0)
	global_store_dwordx4 v[12:13], v[2:5], off
	s_add_i32 s28, s20, 0x90
	v_mov_b32_e32 v10, 0
	v_mov_b32_e32 v4, 0
	v_mov_b32_e32 v5, 0
	v_cvt_pk_fp8_f32 v4, v54, v55
	v_cvt_pk_fp8_f32 v5, v62, v63
	v_mov_b32_e32 v11, 0
	s_ashr_i32 s29, s28, 31
	v_cvt_pk_fp8_f32 v10, v74, v75
	v_cvt_pk_fp8_f32 v11, v78, v79
	ds_read_b128 v[6:9], v198 offset:1024
	v_lshl_add_u64 v[2:3], s[28:29], 0, v[174:175]
	v_lshlrev_b64 v[2:3], 11, v[2:3]
	v_lshl_add_u64 v[2:3], s[8:9], 0, v[2:3]
	v_cvt_pk_fp8_f32 v4, v56, v57 op_sel:[0,0,1]
	v_cvt_pk_fp8_f32 v5, v64, v65 op_sel:[0,0,1]
	v_lshl_add_u64 v[2:3], v[2:3], 0, s[22:23]
	v_cvt_pk_fp8_f32 v10, v76, v77 op_sel:[0,0,1]
	v_cvt_pk_fp8_f32 v11, v80, v81 op_sel:[0,0,1]
	v_lshl_add_u64 v[2:3], v[2:3], 0, v[176:177]
	s_waitcnt lgkmcnt(0)
	global_store_dwordx4 v[2:3], v[6:9], off
	ds_write_b64 v197, v[4:5]
	ds_write_b64 v255, v[10:11]
	v_mov_b32_e32 v8, 0
	v_mov_b32_e32 v9, 0
	v_cvt_pk_fp8_f32 v8, v42, v43
	v_cvt_pk_fp8_f32 v9, v46, v47
	v_mov_b32_e32 v10, 0
	v_mov_b32_e32 v11, 0
	v_cvt_pk_fp8_f32 v10, v50, v51
	v_cvt_pk_fp8_f32 v11, v58, v59
	s_add_i32 s28, s20, 0xa0
	s_ashr_i32 s29, s28, 31
	ds_read_b128 v[2:5], v198
	v_lshl_add_u64 v[6:7], s[28:29], 0, v[174:175]
	v_cvt_pk_fp8_f32 v8, v44, v45 op_sel:[0,0,1]
	v_cvt_pk_fp8_f32 v9, v48, v49 op_sel:[0,0,1]
	v_lshlrev_b64 v[6:7], 11, v[6:7]
	v_cvt_pk_fp8_f32 v10, v52, v53 op_sel:[0,0,1]
	v_cvt_pk_fp8_f32 v11, v60, v61 op_sel:[0,0,1]
	v_lshl_add_u64 v[6:7], s[8:9], 0, v[6:7]
	v_lshl_add_u64 v[6:7], v[6:7], 0, s[22:23]
	s_addk_i32 s20, 0xb0
	v_lshl_add_u64 v[12:13], v[6:7], 0, v[176:177]
	ds_write_b64 v197, v[8:9] offset:1024
	ds_write_b64 v255, v[10:11] offset:1024
	s_ashr_i32 s21, s20, 31
	ds_read_b128 v[6:9], v198 offset:1024
	s_waitcnt lgkmcnt(0)
	global_store_dwordx4 v[12:13], v[2:5], off
	s_andn2_b64 vcc, exec, s[26:27]
	s_nop 0
	v_lshl_add_u64 v[2:3], s[20:21], 0, v[174:175]
	v_lshlrev_b64 v[2:3], 11, v[2:3]
	v_lshl_add_u64 v[2:3], s[8:9], 0, v[2:3]
	v_lshl_add_u64 v[2:3], v[2:3], 0, s[22:23]
	v_lshl_add_u64 v[2:3], v[2:3], 0, v[176:177]
	s_mov_b64 s[20:21], -1
	global_store_dwordx4 v[2:3], v[6:9], off
	s_cbranch_vccnz .LBB0_1946
	s_andn2_b64 vcc, exec, s[6:7]
	s_cbranch_vccnz .LBB0_1945
	s_barrier
	s_branch .LBB0_1945

; #define LAS __attribute__((address_space(3)))
; #define PG8_STAGE(bufoff, gbase, voff) do { _Pragma("unroll") for (int _i = 0; _i < 2; ++_i) \
;         __builtin_amdgcn_global_load_lds((const GAS unsigned*)((const GAS char*)(gbase) + (voff)[_i]), (LAS unsigned*)(lds + (bufoff) + ldsw + _i * 8192), 16, 0, 0); } while (0)
; #define PG8_WAIT_V(n) asm volatile("s_waitcnt vmcnt(" #n ")" ::: "memory")
; #define PG8_BAR __builtin_amdgcn_s_barrier()
; template <class Epi, class Sched, bool GATHER, bool FP8 = false, bool UNI = false>
; __device__ __forceinline__ void gemm_phase(LAS unsigned char* lds, const Sched& S, const Epi& E) {
;     ...
;         PG8_STAGE(PG8_SB(0, 0), cB, boc); PG8_STAGE(PG8_SB(0, 1), cB + hB, boc); PG8_STAGE(PG8_SA(0, 0), cA, aoc[0]); PG8_STAGE(PG8_SA(0, 1), cA, aoc[1]);
;         if (wr == 1) PG8_BAR;
;         PG8_WAIT_V(2); PG8_BAR;
;         PG8_STAGE(PG8_SB(1, 0), cB + 128, boc); PG8_STAGE(PG8_SA(1, 0), cA + 128, aoc[0]); PG8_STAGE(PG8_SB(1, 1), cB + hB + 128, boc);
;         PG8_WAIT_V(6); PG8_BAR;
;     __device__ __forceinline__ bool operator()(f32x4 (&acc)[2][2][4][2], const Unit& u, int wr, int wc, int fr, int fq, LAS unsigned char* scr) const {
;         const int lane = fq * 16 + fr, rowb = u.row0 + wr * 64, colb = u.col0 + wc * 64;
; #pragma unroll
;         for (int ai = 0; ai < 2; ++ai)
; #pragma unroll
;             for (int m = 0; m < 4; ++m) { const size_t rg = (size_t)(rowb + ai * 128 + m * 16);
;                 if constexpr (F8OUT) {
;                     LAS unsigned char* sb = scr + ((ai * 4 + m) & 1) * 1024;
; #pragma unroll
;                     for (int bj = 0; bj < 2; ++bj) { const f32x4 v0 = acc[ai][bj][m][0], v1 = acc[ai][bj][m][1]; u32x2 w8;
;                         int q = __builtin_amdgcn_cvt_pk_fp8_f32(v0[0], v0[1], 0, false); q = __builtin_amdgcn_cvt_pk_fp8_f32(v0[2], v0[3], q, true); w8.x = (unsigned)q;
;                         q = __builtin_amdgcn_cvt_pk_fp8_f32(v1[0], v1[1], 0, false); q = __builtin_amdgcn_cvt_pk_fp8_f32(v1[2], v1[3], q, true); w8.y = (unsigned)q;
;                         *(LAS u32x2*)(sb + fr * 64 + bj * 32 + fq * 8) = w8; }
;                     const int r = lane >> 2, ch = lane & 3; const u32x4 o = *(const LAS u32x4*)(sb + r * 64 + ch * 16);
.LBB0_3172:
	s_lshl_b32 s68, s12, 8
	s_lshl_b32 s69, s10, 8
	s_and_b32 s29, s15, 3
	s_lshl_b32 s49, s19, 6
	s_add_u32 s8, s8, 0x3fb00000
	s_addc_u32 s9, s9, 0
	s_add_i32 s30, s16, 0x18000
	s_add_i32 s50, s30, s26
	s_mov_b64 s[10:11], 0x80
	v_lshl_add_u64 v[8:9], v[8:9], 0, s[10:11]
	s_mov_b32 m0, s50
	s_add_i32 s51, s50, 0x2000
	s_add_i32 s56, s45, 0x8000
	s_add_i32 s57, s45, 0xa000
	s_waitcnt vmcnt(2)
	s_barrier
	global_load_lds_dwordx4 v[8:9], off
	v_lshl_add_u64 v[6:7], v[6:7], 0, s[10:11]
	s_mov_b32 m0, s51
	s_add_u32 s12, s22, 0x4080
	global_load_lds_dwordx4 v[6:7], off
	v_lshl_add_u64 v[2:3], v[2:3], 0, s[10:11]
	s_mov_b32 m0, s56
	s_addc_u32 s13, s23, 0
	s_add_i32 s31, s16, 0x1c000
	global_load_lds_dwordx4 v[2:3], off
	v_lshl_add_u64 v[2:3], v[4:5], 0, s[10:11]
	s_mov_b32 m0, s57
	s_add_i32 s58, s31, s26
	global_load_lds_dwordx4 v[2:3], off
	v_lshl_add_u64 v[2:3], s[12:13], 0, v[162:163]
	s_mov_b32 m0, s58
	s_add_i32 s59, s58, 0x2000
	global_load_lds_dwordx4 v[2:3], off
	v_lshl_add_u64 v[2:3], s[12:13], 0, v[168:169]
	s_mov_b32 m0, s59
	v_lshlrev_b32_e32 v5, 1, v1
	global_load_lds_dwordx4 v[2:3], off
	v_lshlrev_b32_e32 v3, 6, v1
	s_cmpk_lt_u32 s14, 0x100
	v_and_b32_e32 v3, 0x3c0, v3
	v_lshlrev_b32_e32 v4, 2, v1
	v_and_b32_e32 v5, 32, v5
	v_lshlrev_b32_e32 v7, 5, v1
	s_cselect_b64 s[12:13], -1, 0
	s_lshl_b32 s14, s15, 11
	v_and_b32_e32 v4, 32, v4
	v_or_b32_e32 v6, v3, v5
	v_and_b32_e32 v7, 0x400, v7
	s_add_i32 s14, s16, s14
	v_lshrrev_b32_e32 v2, 1, v1
	v_lshl_or_b32 v8, s19, 13, v7
	v_bitop3_b32 v5, v3, v4, v5 bitop3:0x36
	v_bitop3_b32 v4, v6, v4, 16 bitop3:0x36
	v_lshl_or_b32 v7, s29, 12, v7
	s_waitcnt vmcnt(6)
	s_add_i32 s14, s14, 0x20000
	s_lshl_b32 s60, s29, 6
	v_bfe_u32 v174, v1, 2, 4
	s_add_i32 s61, s16, 0x24104
	s_ashr_i32 s62, s17, 3
	s_and_b32 s63, s18, 7
	s_ashr_i32 s64, s18, 3
	v_and_b32_e32 v2, 24, v2
	v_or_b32_e32 v9, v5, v8
	v_or_b32_e32 v6, v4, v8
	v_or_b32_e32 v5, v5, v7
	v_or_b32_e32 v4, v4, v7
	v_and_b32_e32 v176, 48, v10
	v_add_u32_e32 v3, s14, v3
	v_lshl_add_u32 v7, v174, 6, s14
	s_cmp_lt_i32 s64, s62
	v_mov_b32_e32 v167, v163
	v_mov_b32_e32 v173, v163
	v_mov_b32_e32 v175, v163
	v_mov_b32_e32 v177, v163
	s_mov_b32 s65, 0
	s_cselect_b64 s[14:15], -1, 0
	v_add_u32_e32 v1, s27, v5
	v_add_u32_e32 v186, s27, v4
	v_add_u32_e32 v187, s28, v5
	v_add_u32_e32 v188, s28, v4
	v_add_u32_e32 v189, s16, v9
	v_add_u32_e32 v190, s16, v6
	v_mov_b32_e32 v191, 0x79
	v_mov_b32_e32 v192, 0x7f
	v_add_u32_e32 v193, s30, v5
	v_add_u32_e32 v194, s30, v4
	v_add_u32_e32 v195, s31, v5
	v_add_u32_e32 v196, s31, v4
	v_mbcnt_lo_u32_b32 v255, -1, 0
	v_mbcnt_hi_u32_b32 v255, -1, v255
	v_and_b32_e32 v255, 16, v255
	v_xor_b32_e32 v1, v1, v255
	v_xor_b32_e32 v186, v186, v255
	v_xor_b32_e32 v187, v187, v255
	v_xor_b32_e32 v188, v188, v255
	v_xor_b32_e32 v189, v189, v255
	v_xor_b32_e32 v190, v190, v255
	v_xor_b32_e32 v193, v193, v255
	v_xor_b32_e32 v194, v194, v255
	v_xor_b32_e32 v195, v195, v255
	v_xor_b32_e32 v196, v196, v255
	v_add_u32_e32 v197, v3, v2
	v_add_u32_e32 v198, v7, v176
	v_lshrrev_b32_e32 v255, 3, v197
	v_and_b32_e32 v255, 0x30, v255
	v_xor_b32_e32 v197, v197, v255
	v_lshrrev_b32_e32 v255, 3, v198
	v_and_b32_e32 v255, 0x30, v255
	v_xor_b32_e32 v198, v198, v255
	v_xor_b32_e32 v255, 32, v197
	s_barrier
	s_branch .LBB0_3175
